# v35 + instruction selection in GEMM unit headers: the 128 accumulator clears become 64 v_mov_b64 (7 GEMM instances)
# baseline (speedup 1.0000x reference)
.LBB0_350:
	v_mov_b64_e32 v[0:1], 0x6c0
	v_cmp_lt_i64_e32 vcc, s[6:7], v[0:1]
	s_lshl_b32 s34, s31, 19
	s_and_b64 s[6:7], vcc, exec
	s_cselect_b32 s6, s34, s10
	s_lshl_b32 s35, s30, 19
	s_and_b64 s[40:41], vcc, exec
	v_mov_b32_e32 v213, 0x3ba10414
	v_mov_b32_e32 v252, 2
	s_cselect_b32 s7, s35, s39
	s_add_i32 s38, s10, 0x40080
	s_addk_i32 s39, 0x100
	s_mov_b32 s40, -2
	v_mov_b64_e32 v[0:1], 0
	v_mov_b64_e32 v[2:3], 0
	v_mov_b64_e32 v[4:5], 0
	v_mov_b64_e32 v[6:7], 0
	v_mov_b64_e32 v[8:9], 0
	v_mov_b64_e32 v[10:11], 0
	v_mov_b64_e32 v[208:209], 0
	v_mov_b64_e32 v[210:211], 0
	v_mov_b64_e32 v[24:25], 0
	v_mov_b64_e32 v[26:27], 0
	v_mov_b64_e32 v[32:33], 0
	v_mov_b64_e32 v[34:35], 0
	v_mov_b64_e32 v[40:41], 0
	v_mov_b64_e32 v[42:43], 0
	v_mov_b64_e32 v[48:49], 0
	v_mov_b64_e32 v[50:51], 0
	v_mov_b64_e32 v[12:13], 0
	v_mov_b64_e32 v[14:15], 0
	v_mov_b64_e32 v[20:21], 0
	v_mov_b64_e32 v[22:23], 0
	v_mov_b64_e32 v[28:29], 0
	v_mov_b64_e32 v[30:31], 0
	v_mov_b64_e32 v[36:37], 0
	v_mov_b64_e32 v[38:39], 0
	v_mov_b64_e32 v[44:45], 0
	v_mov_b64_e32 v[46:47], 0
	v_mov_b64_e32 v[52:53], 0
	v_mov_b64_e32 v[54:55], 0
	v_mov_b64_e32 v[56:57], 0
	v_mov_b64_e32 v[58:59], 0
	v_mov_b64_e32 v[60:61], 0
	v_mov_b64_e32 v[62:63], 0
	v_mov_b64_e32 v[16:17], 0
	v_mov_b64_e32 v[18:19], 0
	v_mov_b64_e32 v[68:69], 0
	v_mov_b64_e32 v[70:71], 0
	v_mov_b64_e32 v[72:73], 0
	v_mov_b64_e32 v[74:75], 0
	v_mov_b64_e32 v[76:77], 0
	v_mov_b64_e32 v[78:79], 0
	v_mov_b64_e32 v[88:89], 0
	v_mov_b64_e32 v[90:91], 0
	v_mov_b64_e32 v[92:93], 0
	v_mov_b64_e32 v[94:95], 0
	v_mov_b64_e32 v[106:107], 0
	v_mov_b64_e32 v[108:109], 0
	v_mov_b64_e32 v[110:111], 0
	v_mov_b64_e32 v[112:113], 0
	v_mov_b64_e32 v[80:81], 0
	v_mov_b64_e32 v[82:83], 0
	v_mov_b64_e32 v[84:85], 0
	v_mov_b64_e32 v[86:87], 0
	v_mov_b64_e32 v[98:99], 0
	v_mov_b64_e32 v[100:101], 0
	v_mov_b64_e32 v[102:103], 0
	v_mov_b64_e32 v[104:105], 0
	v_mov_b64_e32 v[114:115], 0
	v_mov_b64_e32 v[116:117], 0
	v_mov_b64_e32 v[118:119], 0
	v_mov_b64_e32 v[120:121], 0
	v_mov_b64_e32 v[122:123], 0
	v_mov_b64_e32 v[124:125], 0
	v_mov_b64_e32 v[126:127], 0
	v_mov_b64_e32 v[128:129], 0

.LBB0_483:
	v_mov_b64_e32 v[0:1], 0xd8
	v_cmp_lt_i64_e32 vcc, s[6:7], v[0:1]
	s_mul_i32 s38, s37, 0x300000
	s_and_b64 s[6:7], vcc, exec
	s_cselect_b32 s6, s38, s11
	s_lshl_b32 s39, s36, 18
	s_and_b64 s[42:43], vcc, exec
	s_cselect_b32 s7, s39, s10
	s_add_i32 s42, s11, 0x180080
	s_add_i32 s43, s10, 0x100
	s_mov_b32 s44, -2
	v_mov_b64_e32 v[0:1], 0
	v_mov_b64_e32 v[2:3], 0
	v_mov_b64_e32 v[4:5], 0
	v_mov_b64_e32 v[6:7], 0
	v_mov_b64_e32 v[8:9], 0
	v_mov_b64_e32 v[10:11], 0
	v_mov_b64_e32 v[12:13], 0
	v_mov_b64_e32 v[14:15], 0
	v_mov_b64_e32 v[24:25], 0
	v_mov_b64_e32 v[26:27], 0
	v_mov_b64_e32 v[28:29], 0
	v_mov_b64_e32 v[30:31], 0
	v_mov_b64_e32 v[40:41], 0
	v_mov_b64_e32 v[42:43], 0
	v_mov_b64_e32 v[44:45], 0
	v_mov_b64_e32 v[46:47], 0
	v_mov_b64_e32 v[16:17], 0
	v_mov_b64_e32 v[18:19], 0
	v_mov_b64_e32 v[20:21], 0
	v_mov_b64_e32 v[22:23], 0
	v_mov_b64_e32 v[32:33], 0
	v_mov_b64_e32 v[34:35], 0
	v_mov_b64_e32 v[36:37], 0
	v_mov_b64_e32 v[38:39], 0
	v_mov_b64_e32 v[48:49], 0
	v_mov_b64_e32 v[50:51], 0
	v_mov_b64_e32 v[52:53], 0
	v_mov_b64_e32 v[54:55], 0
	v_mov_b64_e32 v[56:57], 0
	v_mov_b64_e32 v[58:59], 0
	v_mov_b64_e32 v[60:61], 0
	v_mov_b64_e32 v[62:63], 0
	v_mov_b64_e32 v[64:65], 0
	v_mov_b64_e32 v[66:67], 0
	v_mov_b64_e32 v[68:69], 0
	v_mov_b64_e32 v[70:71], 0
	v_mov_b64_e32 v[72:73], 0
	v_mov_b64_e32 v[74:75], 0
	v_mov_b64_e32 v[76:77], 0
	v_mov_b64_e32 v[78:79], 0
	v_mov_b64_e32 v[88:89], 0
	v_mov_b64_e32 v[90:91], 0
	v_mov_b64_e32 v[92:93], 0
	v_mov_b64_e32 v[94:95], 0
	v_mov_b64_e32 v[106:107], 0
	v_mov_b64_e32 v[108:109], 0
	v_mov_b64_e32 v[110:111], 0
	v_mov_b64_e32 v[112:113], 0
	v_mov_b64_e32 v[80:81], 0
	v_mov_b64_e32 v[82:83], 0
	v_mov_b64_e32 v[84:85], 0
	v_mov_b64_e32 v[86:87], 0
	v_mov_b64_e32 v[98:99], 0
	v_mov_b64_e32 v[100:101], 0
	v_mov_b64_e32 v[102:103], 0
	v_mov_b64_e32 v[104:105], 0
	v_mov_b64_e32 v[114:115], 0
	v_mov_b64_e32 v[116:117], 0
	v_mov_b64_e32 v[118:119], 0
	v_mov_b64_e32 v[120:121], 0
	v_mov_b64_e32 v[122:123], 0
	v_mov_b64_e32 v[124:125], 0
	v_mov_b64_e32 v[126:127], 0
	v_mov_b64_e32 v[128:129], 0

.LBB0_1357:
	v_mov_b64_e32 v[0:1], s[12:13]
	v_cmp_lt_i64_e32 vcc, s[10:11], v[0:1]
	s_lshl_b32 s19, s18, 20
	s_lshl_b32 s10, s16, 10
	s_add_i32 s19, s19, s10
	s_and_b64 s[10:11], vcc, exec
	s_cselect_b32 s15, s19, s45
	s_lshl_b32 s43, s17, 18
	s_lshl_b32 s10, s16, 21
	s_add_i32 s43, s43, s10
	s_and_b64 s[10:11], vcc, exec
	s_cselect_b32 s44, s43, s46
	s_add_i32 s45, s45, 0x80080
	s_addk_i32 s46, 0x100
	s_mov_b32 s47, -2
	v_mov_b64_e32 v[0:1], 0
	v_mov_b64_e32 v[2:3], 0
	v_mov_b64_e32 v[4:5], 0
	v_mov_b64_e32 v[6:7], 0
	v_mov_b64_e32 v[8:9], 0
	v_mov_b64_e32 v[10:11], 0
	v_mov_b64_e32 v[12:13], 0
	v_mov_b64_e32 v[14:15], 0
	v_mov_b64_e32 v[24:25], 0
	v_mov_b64_e32 v[26:27], 0
	v_mov_b64_e32 v[28:29], 0
	v_mov_b64_e32 v[30:31], 0
	v_mov_b64_e32 v[40:41], 0
	v_mov_b64_e32 v[42:43], 0
	v_mov_b64_e32 v[44:45], 0
	v_mov_b64_e32 v[46:47], 0
	v_mov_b64_e32 v[16:17], 0
	v_mov_b64_e32 v[18:19], 0
	v_mov_b64_e32 v[20:21], 0
	v_mov_b64_e32 v[22:23], 0
	v_mov_b64_e32 v[32:33], 0
	v_mov_b64_e32 v[34:35], 0
	v_mov_b64_e32 v[36:37], 0
	v_mov_b64_e32 v[38:39], 0
	v_mov_b64_e32 v[48:49], 0
	v_mov_b64_e32 v[50:51], 0
	v_mov_b64_e32 v[52:53], 0
	v_mov_b64_e32 v[54:55], 0
	v_mov_b64_e32 v[56:57], 0
	v_mov_b64_e32 v[58:59], 0
	v_mov_b64_e32 v[60:61], 0
	v_mov_b64_e32 v[62:63], 0
	v_mov_b64_e32 v[64:65], 0
	v_mov_b64_e32 v[66:67], 0
	v_mov_b64_e32 v[68:69], 0
	v_mov_b64_e32 v[70:71], 0
	v_mov_b64_e32 v[72:73], 0
	v_mov_b64_e32 v[74:75], 0
	v_mov_b64_e32 v[76:77], 0
	v_mov_b64_e32 v[78:79], 0
	v_mov_b64_e32 v[88:89], 0
	v_mov_b64_e32 v[90:91], 0
	v_mov_b64_e32 v[92:93], 0
	v_mov_b64_e32 v[94:95], 0
	v_mov_b64_e32 v[106:107], 0
	v_mov_b64_e32 v[108:109], 0
	v_mov_b64_e32 v[110:111], 0
	v_mov_b64_e32 v[112:113], 0
	v_mov_b64_e32 v[80:81], 0
	v_mov_b64_e32 v[82:83], 0
	v_mov_b64_e32 v[84:85], 0
	v_mov_b64_e32 v[86:87], 0
	v_mov_b64_e32 v[98:99], 0
	v_mov_b64_e32 v[100:101], 0
	v_mov_b64_e32 v[102:103], 0
	v_mov_b64_e32 v[104:105], 0
	v_mov_b64_e32 v[114:115], 0
	v_mov_b64_e32 v[116:117], 0
	v_mov_b64_e32 v[118:119], 0
	v_mov_b64_e32 v[120:121], 0
	v_mov_b64_e32 v[122:123], 0
	v_mov_b64_e32 v[124:125], 0
	v_mov_b64_e32 v[126:127], 0
	v_mov_b64_e32 v[128:129], 0

.LBB0_1426:
	v_mov_b64_e32 v[0:1], s[6:7]
	v_cmp_lt_i64_e32 vcc, s[10:11], v[0:1]
	s_lshl_b32 s22, s21, 19
	s_and_b64 s[10:11], vcc, exec
	s_cselect_b32 s19, s22, s46
	s_lshl_b32 s23, s20, 19
	s_and_b64 s[10:11], vcc, exec
	s_cselect_b32 s45, s23, s47
	s_add_i32 s46, s46, 0x40080
	s_addk_i32 s47, 0x100
	s_mov_b32 s48, -2
	v_mov_b64_e32 v[0:1], 0
	v_mov_b64_e32 v[2:3], 0
	v_mov_b64_e32 v[4:5], 0
	v_mov_b64_e32 v[6:7], 0
	s_waitcnt vmcnt(14)
	v_mov_b64_e32 v[16:17], 0
	v_mov_b64_e32 v[18:19], 0
	v_mov_b64_e32 v[20:21], 0
	v_mov_b64_e32 v[22:23], 0
	v_mov_b64_e32 v[32:33], 0
	v_mov_b64_e32 v[34:35], 0
	v_mov_b64_e32 v[36:37], 0
	v_mov_b64_e32 v[38:39], 0
	v_mov_b64_e32 v[48:49], 0
	v_mov_b64_e32 v[50:51], 0
	v_mov_b64_e32 v[52:53], 0
	v_mov_b64_e32 v[54:55], 0
	v_mov_b64_e32 v[8:9], 0
	v_mov_b64_e32 v[10:11], 0
	v_mov_b64_e32 v[12:13], 0
	v_mov_b64_e32 v[14:15], 0
	v_mov_b64_e32 v[24:25], 0
	v_mov_b64_e32 v[26:27], 0
	v_mov_b64_e32 v[28:29], 0
	v_mov_b64_e32 v[30:31], 0
	v_mov_b64_e32 v[40:41], 0
	v_mov_b64_e32 v[42:43], 0
	v_mov_b64_e32 v[44:45], 0
	v_mov_b64_e32 v[46:47], 0
	v_mov_b64_e32 v[56:57], 0
	v_mov_b64_e32 v[58:59], 0
	v_mov_b64_e32 v[60:61], 0
	v_mov_b64_e32 v[62:63], 0
	v_mov_b64_e32 v[64:65], 0
	v_mov_b64_e32 v[66:67], 0
	v_mov_b64_e32 v[68:69], 0
	v_mov_b64_e32 v[70:71], 0
	v_mov_b64_e32 v[98:99], 0
	v_mov_b64_e32 v[100:101], 0
	v_mov_b64_e32 v[102:103], 0
	v_mov_b64_e32 v[104:105], 0
	v_mov_b64_e32 v[114:115], 0
	v_mov_b64_e32 v[116:117], 0
	v_mov_b64_e32 v[118:119], 0
	v_mov_b64_e32 v[120:121], 0
	v_mov_b64_e32 v[130:131], 0
	v_mov_b64_e32 v[132:133], 0
	v_mov_b64_e32 v[134:135], 0
	v_mov_b64_e32 v[136:137], 0
	v_mov_b64_e32 v[80:81], 0
	v_mov_b64_e32 v[82:83], 0
	v_mov_b64_e32 v[92:93], 0
	v_mov_b64_e32 v[94:95], 0
	v_mov_b64_e32 v[106:107], 0
	v_mov_b64_e32 v[108:109], 0
	v_mov_b64_e32 v[110:111], 0
	v_mov_b64_e32 v[112:113], 0
	v_mov_b64_e32 v[122:123], 0
	v_mov_b64_e32 v[124:125], 0
	v_mov_b64_e32 v[126:127], 0
	v_mov_b64_e32 v[128:129], 0
	v_mov_b64_e32 v[138:139], 0
	v_mov_b64_e32 v[140:141], 0
	v_mov_b64_e32 v[142:143], 0
	v_mov_b64_e32 v[144:145], 0

.LBB0_1495:
	v_mov_b64_e32 v[0:1], s[18:19]
	v_cmp_lt_i64_e32 vcc, s[10:11], v[0:1]
	s_lshl_b32 s22, s21, 20
	s_and_b64 s[10:11], vcc, exec
	s_cselect_b32 s48, s22, s50
	s_lshl_b32 s23, s20, 20
	s_and_b64 s[10:11], vcc, exec
	s_cselect_b32 s49, s23, s51
	s_add_i32 s50, s50, 0x80080
	s_addk_i32 s51, 0x100
	s_mov_b32 s52, -2
	v_mov_b64_e32 v[0:1], 0
	v_mov_b64_e32 v[2:3], 0
	v_mov_b64_e32 v[4:5], 0
	v_mov_b64_e32 v[6:7], 0
	v_mov_b64_e32 v[12:13], 0
	v_mov_b64_e32 v[14:15], 0
	s_waitcnt vmcnt(15)
	v_mov_b64_e32 v[20:21], 0
	v_mov_b64_e32 v[22:23], 0
	v_mov_b64_e32 v[48:49], 0
	v_mov_b64_e32 v[50:51], 0
	v_mov_b64_e32 v[52:53], 0
	v_mov_b64_e32 v[54:55], 0
	v_mov_b64_e32 v[56:57], 0
	v_mov_b64_e32 v[58:59], 0
	s_waitcnt vmcnt(14)
	v_mov_b64_e32 v[60:61], 0
	v_mov_b64_e32 v[62:63], 0
	v_mov_b64_e32 v[8:9], 0
	v_mov_b64_e32 v[10:11], 0
	v_mov_b64_e32 v[16:17], 0
	v_mov_b64_e32 v[18:19], 0
	v_mov_b64_e32 v[24:25], 0
	v_mov_b64_e32 v[26:27], 0
	v_mov_b64_e32 v[28:29], 0
	v_mov_b64_e32 v[30:31], 0
	v_mov_b64_e32 v[64:65], 0
	v_mov_b64_e32 v[66:67], 0
	v_mov_b64_e32 v[68:69], 0
	v_mov_b64_e32 v[70:71], 0
	v_mov_b64_e32 v[72:73], 0
	v_mov_b64_e32 v[74:75], 0
	v_mov_b64_e32 v[76:77], 0
	v_mov_b64_e32 v[78:79], 0
	v_mov_b64_e32 v[80:81], 0
	v_mov_b64_e32 v[82:83], 0
	v_mov_b64_e32 v[84:85], 0
	v_mov_b64_e32 v[86:87], 0
	v_mov_b64_e32 v[88:89], 0
	v_mov_b64_e32 v[90:91], 0
	v_mov_b64_e32 v[92:93], 0
	v_mov_b64_e32 v[94:95], 0
	v_mov_b64_e32 v[114:115], 0
	v_mov_b64_e32 v[116:117], 0
	v_mov_b64_e32 v[118:119], 0
	v_mov_b64_e32 v[120:121], 0
	v_mov_b64_e32 v[122:123], 0
	v_mov_b64_e32 v[124:125], 0
	v_mov_b64_e32 v[126:127], 0
	v_mov_b64_e32 v[128:129], 0
	v_mov_b64_e32 v[98:99], 0
	v_mov_b64_e32 v[100:101], 0
	v_mov_b64_e32 v[102:103], 0
	v_mov_b64_e32 v[104:105], 0
	v_mov_b64_e32 v[106:107], 0
	v_mov_b64_e32 v[108:109], 0
	v_mov_b64_e32 v[110:111], 0
	v_mov_b64_e32 v[112:113], 0
	v_mov_b64_e32 v[130:131], 0
	v_mov_b64_e32 v[132:133], 0
	v_mov_b64_e32 v[134:135], 0
	v_mov_b64_e32 v[136:137], 0
	v_mov_b64_e32 v[138:139], 0
	v_mov_b64_e32 v[140:141], 0
	v_mov_b64_e32 v[142:143], 0
	v_mov_b64_e32 v[144:145], 0

.LBB0_1513:
	v_mov_b64_e32 v[0:1], s[18:19]
	v_cmp_lt_i64_e32 vcc, s[10:11], v[0:1]
	s_lshl_b32 s16, s15, 20
	s_and_b64 s[10:11], vcc, exec
	s_cselect_b32 s47, s16, s49
	s_lshl_b32 s17, s14, 20
	s_and_b64 s[10:11], vcc, exec
	s_cselect_b32 s48, s17, s50
	s_add_i32 s49, s49, 0x80080
	s_addk_i32 s50, 0x100
	s_mov_b32 s51, -2
	v_mov_b64_e32 v[0:1], 0
	v_mov_b64_e32 v[2:3], 0
	v_mov_b64_e32 v[4:5], 0
	v_mov_b64_e32 v[6:7], 0
	v_mov_b64_e32 v[8:9], 0
	v_mov_b64_e32 v[10:11], 0
	v_mov_b64_e32 v[12:13], 0
	v_mov_b64_e32 v[14:15], 0
	v_mov_b64_e32 v[32:33], 0
	v_mov_b64_e32 v[34:35], 0
	v_mov_b64_e32 v[36:37], 0
	v_mov_b64_e32 v[38:39], 0
	v_mov_b64_e32 v[40:41], 0
	v_mov_b64_e32 v[42:43], 0
	v_mov_b64_e32 v[44:45], 0
	v_mov_b64_e32 v[46:47], 0
	s_waitcnt vmcnt(14)
	v_mov_b64_e32 v[16:17], 0
	v_mov_b64_e32 v[18:19], 0
	v_mov_b64_e32 v[20:21], 0
	v_mov_b64_e32 v[22:23], 0
	v_mov_b64_e32 v[24:25], 0
	v_mov_b64_e32 v[26:27], 0
	v_mov_b64_e32 v[28:29], 0
	v_mov_b64_e32 v[30:31], 0
	v_mov_b64_e32 v[48:49], 0
	v_mov_b64_e32 v[50:51], 0
	v_mov_b64_e32 v[52:53], 0
	v_mov_b64_e32 v[54:55], 0
	v_mov_b64_e32 v[56:57], 0
	v_mov_b64_e32 v[58:59], 0
	v_mov_b64_e32 v[60:61], 0
	v_mov_b64_e32 v[62:63], 0
	v_mov_b64_e32 v[80:81], 0
	v_mov_b64_e32 v[82:83], 0
	v_mov_b64_e32 v[84:85], 0
	v_mov_b64_e32 v[86:87], 0
	v_mov_b64_e32 v[88:89], 0
	v_mov_b64_e32 v[90:91], 0
	v_mov_b64_e32 v[92:93], 0
	v_mov_b64_e32 v[94:95], 0
	v_mov_b64_e32 v[114:115], 0
	v_mov_b64_e32 v[116:117], 0
	v_mov_b64_e32 v[118:119], 0
	v_mov_b64_e32 v[120:121], 0
	v_mov_b64_e32 v[122:123], 0
	v_mov_b64_e32 v[124:125], 0
	v_mov_b64_e32 v[126:127], 0
	v_mov_b64_e32 v[128:129], 0
	v_mov_b64_e32 v[98:99], 0
	v_mov_b64_e32 v[100:101], 0
	v_mov_b64_e32 v[102:103], 0
	v_mov_b64_e32 v[104:105], 0
	v_mov_b64_e32 v[106:107], 0
	v_mov_b64_e32 v[108:109], 0
	v_mov_b64_e32 v[110:111], 0
	v_mov_b64_e32 v[112:113], 0
	v_mov_b64_e32 v[130:131], 0
	v_mov_b64_e32 v[132:133], 0
	v_mov_b64_e32 v[134:135], 0
	v_mov_b64_e32 v[136:137], 0
	v_mov_b64_e32 v[138:139], 0
	v_mov_b64_e32 v[140:141], 0
	v_mov_b64_e32 v[142:143], 0
	v_mov_b64_e32 v[144:145], 0

.LBB0_1638:
	v_mov_b64_e32 v[0:1], s[6:7]
	v_cmp_lt_i64_e32 vcc, s[10:11], v[0:1]
	s_lshl_b32 s16, s15, 20
	s_and_b64 s[10:11], vcc, exec
	s_cselect_b32 s39, s16, s41
	s_lshl_b32 s17, s14, 20
	s_and_b64 s[10:11], vcc, exec
	s_cselect_b32 s40, s17, s42
	s_add_i32 s41, s41, 0x80080
	s_addk_i32 s42, 0x100
	s_mov_b32 s43, -2
	v_mov_b64_e32 v[0:1], 0
	v_mov_b64_e32 v[2:3], 0
	v_mov_b64_e32 v[12:13], 0
	v_mov_b64_e32 v[14:15], 0
	v_mov_b64_e32 v[4:5], 0
	v_mov_b64_e32 v[6:7], 0
	v_mov_b64_e32 v[20:21], 0
	v_mov_b64_e32 v[22:23], 0
	v_mov_b64_e32 v[8:9], 0
	v_mov_b64_e32 v[10:11], 0
	v_mov_b64_e32 v[24:25], 0
	v_mov_b64_e32 v[26:27], 0
	v_mov_b64_e32 v[16:17], 0
	v_mov_b64_e32 v[18:19], 0
	v_mov_b64_e32 v[28:29], 0
	v_mov_b64_e32 v[30:31], 0
	v_mov_b64_e32 v[36:37], 0
	v_mov_b64_e32 v[38:39], 0
	v_mov_b64_e32 v[52:53], 0
	v_mov_b64_e32 v[54:55], 0
	v_mov_b64_e32 v[44:45], 0
	v_mov_b64_e32 v[46:47], 0
	v_mov_b64_e32 v[68:69], 0
	v_mov_b64_e32 v[70:71], 0
	v_mov_b64_e32 v[56:57], 0
	v_mov_b64_e32 v[58:59], 0
	v_mov_b64_e32 v[80:81], 0
	v_mov_b64_e32 v[82:83], 0
	v_mov_b64_e32 v[72:73], 0
	v_mov_b64_e32 v[74:75], 0
	v_mov_b64_e32 v[88:89], 0
	v_mov_b64_e32 v[90:91], 0
	v_mov_b64_e32 v[32:33], 0
	v_mov_b64_e32 v[34:35], 0
	v_mov_b64_e32 v[60:61], 0
	v_mov_b64_e32 v[62:63], 0
	v_mov_b64_e32 v[40:41], 0
	v_mov_b64_e32 v[42:43], 0
	v_mov_b64_e32 v[76:77], 0
	v_mov_b64_e32 v[78:79], 0
	v_mov_b64_e32 v[48:49], 0
	v_mov_b64_e32 v[50:51], 0
	v_mov_b64_e32 v[84:85], 0
	v_mov_b64_e32 v[86:87], 0
	v_mov_b64_e32 v[64:65], 0
	v_mov_b64_e32 v[66:67], 0
	v_mov_b64_e32 v[92:93], 0
	v_mov_b64_e32 v[94:95], 0
	v_mov_b64_e32 v[98:99], 0
	v_mov_b64_e32 v[100:101], 0
	v_mov_b64_e32 v[110:111], 0
	v_mov_b64_e32 v[112:113], 0
	v_mov_b64_e32 v[102:103], 0
	v_mov_b64_e32 v[104:105], 0
	v_mov_b64_e32 v[118:119], 0
	v_mov_b64_e32 v[120:121], 0
	v_mov_b64_e32 v[106:107], 0
	v_mov_b64_e32 v[108:109], 0
	v_mov_b64_e32 v[122:123], 0
	v_mov_b64_e32 v[124:125], 0
	v_mov_b64_e32 v[114:115], 0
	v_mov_b64_e32 v[116:117], 0
	v_mov_b64_e32 v[126:127], 0
	v_mov_b64_e32 v[128:129], 0
